# norm1/norm2/router rows remapped to XCD-aware blocks; norm1-inproj, outproj-norm2, GU-down barriers XCD-local under runtime placement check
# baseline (speedup 1.0000x reference)
; #define GAS __attribute__((address_space(1)))
; template <int MODE> DI void p_norm(Frame& F, const void* xin, const bool xbf, int comb_l, bf16* xout, const float* wn, const float* shift, const float* scale, bf16* hout, float* fout, const int blk = -1) {
;     const int gw0 = F.vcu * NWAVES + F.wave; const int gw = blk < 0 ? gw0 : blk * 128 + F.wave * 16, NGW = blk < 0 ? F.G * NWAVES : 1, TE = blk < 0 ? T : blk * 128 + F.wave * 16 + 16;
;     const float* mod = (const float*)(F.ws + WS_MOD);
;     const int* tokd = (const int*)(F.ws + WS_TOK + 768 * 1024); const float* tokw = (const float*)(F.ws + WS_TOK + 512 * 1024);
;     ...
;     const bf16* yb = (const bf16*)(F.ws + WS_XB);
;     ...
;     const bf16* yb = (const bf16*)(F.ws + WS_YB);
;     ...
;     const bool comb = comb_l >= 0;
;     f32x4 wv[4];
; #pragma unroll
;     for (int j = 0; j < 4; ++j) wv[j] = *((const f32x4*)wn + F.lane + 64 * j);
;     struct Tok { v2u d, w; };
;     struct Row { v2u xb[4]; f32x4 xf[4]; v2u ya[4], yc[4]; };
;     auto ld_tok = [&](const int m, Tok& t) { t.d = *(const v2u*)(tokd + 2 * m); t.w = *(const v2u*)((const unsigned*)tokw + 2 * m); };
;     auto ld_row = [&](const int m, const Tok& t, Row& R) {
;         if (xbf) { const GAS v2u* xr = (const GAS v2u*)((const bf16*)xin + (size_t)m * D) + F.lane;
; #pragma unroll
;             for (int j = 0; j < 4; ++j) R.xb[j] = __builtin_nontemporal_load(xr + 64 * j);
;         } else { const GAS f32x4* xr = (const GAS f32x4*)((const float*)xin + (size_t)m * D) + F.lane;
; #pragma unroll
;             for (int j = 0; j < 4; ++j) R.xf[j] = __builtin_nontemporal_load(xr + 64 * j); }
;         if (comb) {
; #pragma unroll
;             for (int j = 0; j < 4; ++j) { R.ya[j] = __builtin_nontemporal_load((const v2u*)(yb + (size_t)t.d[0] * 1024) + F.lane + 64 * j); R.yc[j] = __builtin_nontemporal_load((const v2u*)(yb + (size_t)t.d[1] * 1024) + F.lane + 64 * j); } } };
;     Tok tA, tB; Row RA;
;     tA.d = (v2u){0u, 0u}; tA.w = tA.d; tB = tA;
;     if (gw < TE) { if (comb) { ld_tok(gw, tA); if (gw + NGW < TE) ld_tok(gw + NGW, tB); } ld_row(gw, tA, RA); }
;     for (int m = gw; m < TE; m += NGW) {
;         Row RN; Tok tN; tN.d = (v2u){0u, 0u}; tN.w = tN.d;
;         if (m + NGW < TE) { ld_row(m + NGW, tB, RN); if (comb && m + 2 * NGW < TE) ld_tok(m + 2 * NGW, tN); }
.LBB0_362:
	s_add_i32 s2, s2, 0x20888
	v_mov_b32_e32 v0, s2
	s_waitcnt lgkmcnt(0)
	ds_read2_b32 v[4:5], v0 offset1:1
	s_ashr_i32 s21, s4, 6
	s_lshl_b32 s21, s21, 4
	s_lshl_b32 s22, s5, 7
	s_add_i32 s24, s22, s21
	s_add_i32 s40, s24, 15
	s_cmpk_gt_i32 s24, 0x7fff
	s_waitcnt lgkmcnt(0)
	v_readfirstlane_b32 s2, v4
	v_readfirstlane_b32 s3, v5
	s_cbranch_scc1 .LBB0_394
	s_ashr_i32 s11, s10, 31
	s_lshl_b64 s[4:5], s[10:11], 12
	v_and_b32_e32 v1, 63, v1
	s_add_u32 s2, s2, s4
	s_addc_u32 s3, s3, s5
	s_waitcnt vmcnt(0)
	v_lshlrev_b32_e32 v52, 4, v1
	global_load_dwordx4 v[4:7], v52, s[2:3]
	global_load_dwordx4 v[8:11], v52, s[2:3] offset:1024
	global_load_dwordx4 v[12:15], v52, s[2:3] offset:2048
	global_load_dwordx4 v[16:19], v52, s[2:3] offset:3072
	s_add_u32 s30, s28, 0x4c0000
	s_addc_u32 s31, s29, 0
	s_mov_b32 s8, 1
	s_add_u32 s34, s28, 0x480000
	s_addc_u32 s35, s29, 0
	s_cmp_gt_i32 s10, 0
	s_mov_b32 s52, s53
	s_cselect_b64 s[14:15], -1, 0
	s_cmp_lt_i32 s10, 1
	s_cbranch_scc1 .LBB0_367
	s_lshl_b32 s2, s24, 1
	s_ashr_i32 s3, s2, 31
	s_lshl_b64 s[2:3], s[2:3], 2
	s_add_u32 s4, s30, s2
	s_addc_u32 s5, s31, s3
	s_add_u32 s2, s34, s2
	s_addc_u32 s3, s35, s3
	global_load_dwordx2 v[20:21], v3, s[4:5]
	global_load_dwordx2 v[98:99], v3, s[2:3]
	s_add_i32 s2, s24, s8
	s_cmp_gt_i32 s2, s40
	s_cbranch_scc1 .LBB0_368
	s_lshl_b32 s2, s2, 1
	s_ashr_i32 s3, s2, 31
	s_lshl_b64 s[2:3], s[2:3], 2
	s_add_u32 s4, s30, s2
	s_addc_u32 s5, s31, s3
	s_add_u32 s2, s34, s2
	global_load_dwordx2 v[22:23], v3, s[4:5]
	s_addc_u32 s3, s35, s3
	global_load_dwordx2 v[58:59], v3, s[2:3]
	s_waitcnt vmcnt(1)
	v_mov_b32_e32 v56, v23
	v_mov_b32_e32 v2, v22
	s_branch .LBB0_369

; template <int MODE> DI void p_norm(Frame& F, const void* xin, const bool xbf, int comb_l, bf16* xout, const float* wn, const float* shift, const float* scale, bf16* hout, float* fout, const int blk = -1) {
;     ...
;     if (gw < TE) { if (comb) { ld_tok(gw, tA); if (gw + NGW < TE) ld_tok(gw + NGW, tB); } ld_row(gw, tA, RA); }
;     for (int m = gw; m < TE; m += NGW) {
;         Row RN; Tok tN; tN.d = (v2u){0u, 0u}; tN.w = tN.d;
;         if (m + NGW < TE) { ld_row(m + NGW, tB, RN); if (comb && m + 2 * NGW < TE) ld_tok(m + 2 * NGW, tN); }
.LBB0_374:
	s_add_i32 s52, s10, -1
	s_mul_hi_i32 s9, s10, 0x18000
	s_mul_i32 s10, s10, 0x18000
	s_add_u32 s14, s28, s10
	s_addc_u32 s15, s29, s9
	v_mov_b32_e32 v53, v3
	s_waitcnt vmcnt(1)
	v_lshl_add_u64 v[20:21], s[14:15], 0, v[52:53]
	s_mov_b64 s[14:15], 0x101000
	v_lshl_add_u64 v[62:63], v[20:21], 0, s[14:15]
	s_mov_b64 s[14:15], 0x100000
	s_lshl_b64 s[10:11], s[52:53], 2
	v_lshl_add_u64 v[64:65], v[20:21], 0, s[14:15]
	s_lshl_b64 s[14:15], s[24:25], 11
	s_add_u32 s9, s12, s14
	v_readlane_b32 s36, v255, 3
	s_addc_u32 s13, s13, s15
	v_readlane_b32 s38, v255, 5
	v_mov_b32_e32 v55, v3
	v_readlane_b32 s39, v255, 6
	s_add_u32 s12, s38, s9
	v_lshl_add_u64 v[60:61], s[16:17], 0, v[54:55]
	s_addc_u32 s13, s39, s13
	s_add_i32 s16, s21, s8
	s_add_i32 s26, s16, s22
	s_ashr_i32 s9, s8, 31
	s_ashr_i32 s27, s26, 31
	s_lshl_b64 s[14:15], s[8:9], 11
	s_lshl_b64 s[16:17], s[26:27], 12
	s_add_u32 s16, s18, s16
	s_addc_u32 s17, s19, s17
	v_lshl_add_u64 v[20:21], s[16:17], 0, v[52:53]
	s_mov_b64 s[16:17], 0x800
	v_lshl_add_u64 v[66:67], v[20:21], 0, s[16:17]
	s_lshl_b64 s[16:17], s[8:9], 12
	s_lshl_b64 s[26:27], s[26:27], 11
	s_add_u32 s18, s18, s26
	s_addc_u32 s19, s19, s27
	s_mov_b32 s9, 2
	s_add_i32 s20, s21, s9
	v_lshlrev_b32_e32 v0, 2, v1
	s_add_i32 s20, s20, s22
	v_xor_b32_e32 v1, 4, v0
	v_xor_b32_e32 v128, 8, v0
	v_xor_b32_e32 v129, 16, v0
	v_xor_b32_e32 v130, 32, v0
	v_xor_b32_e32 v131, 64, v0
	v_xor_b32_e32 v132, 0x80, v0
	s_lshl_b32 s20, s20, 1
	v_readlane_b32 s37, v255, 4
	s_branch .LBB0_376

; template <int MODE> DI void p_norm(Frame& F, const void* xin, const bool xbf, int comb_l, bf16* xout, const float* wn, const float* shift, const float* scale, bf16* hout, float* fout, const int blk = -1) {
;     ...
;     for (int m = gw; m < TE; m += NGW) {
;         Row RN; Tok tN; tN.d = (v2u){0u, 0u}; tN.w = tN.d;
;         if (m + NGW < TE) { ld_row(m + NGW, tB, RN); if (comb && m + 2 * NGW < TE) ld_tok(m + 2 * NGW, tN); }
.LBB0_376:
	s_add_i32 s25, s24, s8
	s_cmp_gt_i32 s25, s40
	s_cselect_b64 s[22:23], -1, 0
	s_waitcnt vmcnt(0)
	v_mov_b64_e32 v[76:77], v[58:59]
	s_and_b64 vcc, exec, s[22:23]
	s_cbranch_vccnz .LBB0_385
	s_and_b64 vcc, exec, s[2:3]
	s_cbranch_vccnz .LBB0_393
	v_lshl_add_u64 v[58:59], s[18:19], 0, v[54:55]
	global_load_dwordx2 v[114:115], v[58:59], off nt
	global_load_dwordx2 v[112:113], v[58:59], off offset:512 nt
	global_load_dwordx2 v[106:107], v[58:59], off offset:1024 nt
	global_load_dwordx2 v[104:105], v[58:59], off offset:1536 nt
	s_cbranch_execnz .LBB0_380

; template <int MODE> DI void p_norm(Frame& F, const void* xin, const bool xbf, int comb_l, bf16* xout, const float* wn, const float* shift, const float* scale, bf16* hout, float* fout, const int blk = -1) {
;     ...
;         if (m + NGW < TE) { ld_row(m + NGW, tB, RN); if (comb && m + 2 * NGW < TE) ld_tok(m + 2 * NGW, tN); }
.LBB0_382:
	s_mov_b32 s52, s53
	s_and_b64 vcc, exec, s[4:5]
	s_cbranch_vccnz .LBB0_387
	s_add_i32 s21, s9, s24
	s_cmp_gt_i32 s21, s40
	s_cbranch_scc1 .LBB0_387
	s_ashr_i32 s21, s20, 31
	s_lshl_b64 s[26:27], s[20:21], 2
	s_add_u32 s36, s30, s26
	s_addc_u32 s37, s31, s27
	s_add_u32 s26, s34, s26
	global_load_dwordx2 v[86:87], v3, s[36:37]
	s_addc_u32 s27, s35, s27
	global_load_dwordx2 v[58:59], v3, s[26:27]
	s_waitcnt vmcnt(1)
	v_mov_b32_e32 v56, v87
	v_mov_b32_e32 v2, v86
	s_branch .LBB0_388

; #define GAS __attribute__((address_space(1)))
; template <int MODE> DI void p_norm(Frame& F, const void* xin, const bool xbf, int comb_l, bf16* xout, const float* wn, const float* shift, const float* scale, bf16* hout, float* fout, const int blk = -1) {
;     const int gw0 = F.vcu * NWAVES + F.wave; const int gw = blk < 0 ? gw0 : blk * 128 + F.wave * 16, NGW = blk < 0 ? F.G * NWAVES : 1, TE = blk < 0 ? T : blk * 128 + F.wave * 16 + 16;
;     const float* mod = (const float*)(F.ws + WS_MOD);
;     const int* tokd = (const int*)(F.ws + WS_TOK + 768 * 1024); const float* tokw = (const float*)(F.ws + WS_TOK + 512 * 1024);
;     ...
;     const bf16* yb = (const bf16*)(F.ws + WS_XB);
;     ...
;     const bf16* yb = (const bf16*)(F.ws + WS_YB);
;     ...
;     const bool comb = comb_l >= 0;
;     f32x4 wv[4];
; #pragma unroll
;     for (int j = 0; j < 4; ++j) wv[j] = *((const f32x4*)wn + F.lane + 64 * j);
;     struct Tok { v2u d, w; };
;     struct Row { v2u xb[4]; f32x4 xf[4]; v2u ya[4], yc[4]; };
;     auto ld_tok = [&](const int m, Tok& t) { t.d = *(const v2u*)(tokd + 2 * m); t.w = *(const v2u*)((const unsigned*)tokw + 2 * m); };
;     auto ld_row = [&](const int m, const Tok& t, Row& R) {
;         if (xbf) { const GAS v2u* xr = (const GAS v2u*)((const bf16*)xin + (size_t)m * D) + F.lane;
; #pragma unroll
;             for (int j = 0; j < 4; ++j) R.xb[j] = __builtin_nontemporal_load(xr + 64 * j);
;         } else { const GAS f32x4* xr = (const GAS f32x4*)((const float*)xin + (size_t)m * D) + F.lane;
; #pragma unroll
;             for (int j = 0; j < 4; ++j) R.xf[j] = __builtin_nontemporal_load(xr + 64 * j); }
;         if (comb) {
; #pragma unroll
;             for (int j = 0; j < 4; ++j) { R.ya[j] = __builtin_nontemporal_load((const v2u*)(yb + (size_t)t.d[0] * 1024) + F.lane + 64 * j); R.yc[j] = __builtin_nontemporal_load((const v2u*)(yb + (size_t)t.d[1] * 1024) + F.lane + 64 * j); } } };
;     Tok tA, tB; Row RA;
;     tA.d = (v2u){0u, 0u}; tA.w = tA.d; tB = tA;
;     if (gw < TE) { if (comb) { ld_tok(gw, tA); if (gw + NGW < TE) ld_tok(gw + NGW, tB); } ld_row(gw, tA, RA); }
;     for (int m = gw; m < TE; m += NGW) {
;         Row RN; Tok tN; tN.d = (v2u){0u, 0u}; tN.w = tN.d;
;         if (m + NGW < TE) { ld_row(m + NGW, tB, RN); if (comb && m + 2 * NGW < TE) ld_tok(m + 2 * NGW, tN); }
;         const int b = m >> 13;
.LBB0_3232:
	s_add_i32 s8, s8, 0
	s_add_i32 s8, s8, 0x20890
	v_mov_b32_e32 v0, s8
	s_waitcnt lgkmcnt(0)
	ds_read2_b32 v[4:5], v0 offset1:1
	s_ashr_i32 s8, s3, 6
	s_lshl_b32 s8, s8, 4
	s_lshl_b32 s9, s7, 7
	s_add_i32 s12, s9, s8
	s_add_i32 s34, s12, 15
	s_cmpk_gt_i32 s12, 0x7fff
	s_waitcnt lgkmcnt(0)
	v_readfirstlane_b32 s7, v4
	v_readfirstlane_b32 s10, v5
	s_cbranch_scc1 .LBB0_3237
	v_readlane_b32 s16, v255, 3
	v_readlane_b32 s18, v255, 5
	v_readlane_b32 s19, v255, 6
	s_add_u32 s14, s18, s0
	s_addc_u32 s15, s19, s1
	s_ashr_i32 s3, s2, 31
	s_lshl_b64 s[0:1], s[2:3], 12
	s_waitcnt vmcnt(0)
	v_and_b32_e32 v22, 63, v1
	s_add_u32 s0, s7, s0
	s_addc_u32 s1, s10, s1
	v_lshlrev_b32_e32 v2, 4, v22
	global_load_dwordx4 v[4:7], v2, s[0:1]
	global_load_dwordx4 v[8:11], v2, s[0:1] offset:1024
	global_load_dwordx4 v[12:15], v2, s[0:1] offset:2048
	global_load_dwordx4 v[16:19], v2, s[0:1] offset:3072
	s_mov_b32 s0, 1
	s_mul_hi_i32 s1, s2, 0x18000
	s_mul_i32 s2, s2, 0x18000
	s_add_u32 s2, s14, s2
	s_addc_u32 s3, s15, s1
	s_ashr_i32 s13, s12, 31
	s_lshl_b64 s[6:7], s[12:13], 11
	s_add_u32 s6, s14, s6
	s_addc_u32 s7, s15, s7
	v_lshlrev_b32_e32 v24, 3, v22
	v_mov_b32_e32 v25, v3
	v_lshl_add_u64 v[0:1], s[6:7], 0, v[24:25]
	s_mov_b64 s[6:7], 0x3d900000
	s_mov_b32 s1, 0x3d900000
	v_lshl_add_u64 v[20:21], v[0:1], 0, s[6:7]
	v_add_co_u32_e32 v0, vcc, s1, v0
	s_add_i32 s1, s8, s0
	s_nop 0
	v_addc_co_u32_e32 v1, vcc, 0, v1, vcc
	global_load_dwordx2 v[42:43], v[0:1], off nt
	global_load_dwordx2 v[44:45], v[20:21], off offset:512 nt
	global_load_dwordx2 v[40:41], v[20:21], off offset:1024 nt
	global_load_dwordx2 v[36:37], v[20:21], off offset:1536 nt
	v_lshlrev_b32_e32 v0, 2, v22
	v_lshl_add_u64 v[22:23], s[2:3], 0, v[2:3]
	s_mov_b64 s[2:3], 0x104000
	v_lshl_add_u64 v[20:21], v[22:23], 0, s[2:3]
	s_mov_b64 s[2:3], 0x103000
	v_lshl_add_u64 v[22:23], v[22:23], 0, s[2:3]
	s_add_i32 s2, s1, s9
	s_ashr_i32 s3, s2, 31
	s_lshl_b64 s[2:3], s[2:3], 11
	s_add_u32 s2, s2, 0x3d900400
	s_addc_u32 s3, s3, 0
	s_ashr_i32 s1, s0, 31
	s_lshl_b64 s[6:7], s[0:1], 11
	s_ashr_i32 s1, s8, 31
	s_ashr_i32 s10, s9, 31
	s_add_u32 s8, s8, s9
	s_addc_u32 s9, s1, s10
	s_lshl_b64 s[8:9], s[8:9], 11
	s_add_u32 s8, s8, 0x7100400
	v_xor_b32_e32 v1, 4, v0
	v_xor_b32_e32 v56, 8, v0
	v_xor_b32_e32 v57, 16, v0
	v_xor_b32_e32 v58, 32, v0
	v_xor_b32_e32 v59, 64, v0
	v_xor_b32_e32 v60, 0x80, v0
	v_lshl_add_u64 v[24:25], s[14:15], 0, v[24:25]
	s_addc_u32 s9, s9, 0
	v_readlane_b32 s17, v255, 4
	s_branch .LBB0_3235

; DI void p_router(Frame& F, int l) {
;     ...
;     const int r = F.lane & 15, q = F.lane >> 4;
;     tile_g2l(WRL, WRP, WR, 1024, 48, 1024, F.tid);
;     __syncthreads();
;     for (int blk = F.bx; blk < T / 128; blk += F.G) {
;         if (F.tid < 256) CNT[F.tid] = 0;
;         __syncthreads();
;         const int row0 = blk * 128 + F.wave * 16;
.LBB0_3291:
	v_readlane_b32 s2, v255, 10
	s_cmp_le_i32 s2, s50
	s_cselect_b64 s[12:13], -1, 0
	s_and_b64 s[0:1], s[12:13], s[0:1]
	s_andn2_b64 vcc, exec, s[0:1]
	v_readlane_b32 s3, v255, 11
	s_cbranch_vccnz .LBB0_3378
	v_mov_b32_e32 v1, v228
	s_mov_b64 s[0:1], 0
	s_mov_b32 s2, s53
	v_readlane_b32 s52, v255, 2
	s_and_b32 s42, s57, 7
	s_lshl_b32 s42, s42, 5
	s_lshr_b32 s43, s57, 3
	s_add_i32 s42, s42, s43
	v_readlane_b32 s4, v255, 3
	s_add_i32 s94, s2, 0
	v_readlane_b32 s6, v255, 5
	v_readlane_b32 s7, v255, 6
	s_add_u32 s0, s6, s0
	s_movk_i32 s2, 0x1800
	v_readfirstlane_b32 s9, v1
	s_addc_u32 s1, s7, s1
	v_readlane_b32 s8, v255, 19
	v_cmp_gt_i32_e32 vcc, s2, v1
	v_readlane_b32 s5, v255, 4
	s_and_saveexec_b64 s[2:3], vcc
	s_movk_i32 s11, 0x810
	s_cbranch_execz .LBB0_3295
	s_add_u32 s4, s0, 0x700000
	s_addc_u32 s5, s1, 0
	v_lshlrev_b32_e32 v2, 3, v1
	s_waitcnt lgkmcnt(0)
	v_lshl_add_u32 v4, v1, 4, s94
	s_mov_b64 s[6:7], 0
	v_mov_b32_e32 v5, v1
